# adds: XCD leaders skip the now-redundant post-release invalidate and waits
# baseline (speedup 1.0000x reference)
.LBB0_182:
	s_or_b64 exec, exec, s[0:1]
	v_readlane_b32 s0, v254, 59
	v_readlane_b32 s1, v254, 60
.LBB0_183:
	s_or_b64 exec, exec, s[2:3]
	s_waitcnt lgkmcnt(0)
	s_barrier

.LBB0_288:
	s_or_b64 exec, exec, s[0:1]
	v_readlane_b32 s0, v254, 59
	v_readlane_b32 s1, v254, 60
.LBB0_289:
	s_or_b64 exec, exec, s[2:3]
	s_waitcnt lgkmcnt(0)
	s_barrier

.LBB0_361:
	s_or_b64 exec, exec, s[0:1]
	v_readlane_b32 s0, v254, 59
	v_readlane_b32 s1, v254, 60
.LBB0_362:
	s_or_b64 exec, exec, s[2:3]
	s_waitcnt lgkmcnt(0)
	s_barrier

.LBB0_797:
	s_or_b64 exec, exec, s[0:1]
	v_readlane_b32 s0, v254, 59
	v_readlane_b32 s1, v254, 60
.LBB0_798:
	s_or_b64 exec, exec, s[2:3]
	s_waitcnt lgkmcnt(0)
	s_barrier

.LBB0_872:
	s_or_b64 exec, exec, s[0:1]
	v_readlane_b32 s0, v254, 59
	v_readlane_b32 s1, v254, 60
.LBB0_873:
	s_or_b64 exec, exec, s[2:3]
	s_waitcnt lgkmcnt(0)
	s_barrier

.LBB0_983:
	s_or_b64 exec, exec, s[0:1]
	v_readlane_b32 s0, v254, 59
	v_readlane_b32 s1, v254, 60
.LBB0_984:
	s_or_b64 exec, exec, s[2:3]
	s_waitcnt lgkmcnt(0)
	s_barrier

.LBB0_1103:
	s_or_b64 exec, exec, s[0:1]
	v_readlane_b32 s0, v254, 59
	v_readlane_b32 s1, v254, 60
.LBB0_1104:
	s_or_b64 exec, exec, s[2:3]
	s_waitcnt lgkmcnt(0)
	s_barrier

.LBB0_1211:
	s_or_b64 exec, exec, s[0:1]
	v_readlane_b32 s0, v254, 59
	v_readlane_b32 s1, v254, 60
.LBB0_1212:
	s_or_b64 exec, exec, s[2:3]
	s_waitcnt lgkmcnt(0)
	s_barrier

.LBB0_1304:
	s_or_b64 exec, exec, s[0:1]
	v_readlane_b32 s0, v254, 59
	v_readlane_b32 s1, v254, 60
.LBB0_1305:
	s_or_b64 exec, exec, s[2:3]
	s_waitcnt lgkmcnt(0)
	s_barrier
